# att2_kread_batching
# speedup vs baseline: 1.0126x; 1.0067x over previous
; __device__ __forceinline__ void qkt64c(f32x16& p0, f32x16& p1, const char* Ks, const bf16x8* qr, const f32x16& cinit, int r32, int hi) {
; #pragma unroll
;     for (int d0 = 0; d0 < 4; ++d0) { const int cb = (d0 * 16 + hi * 8) * 2;
;         const bf16x8 b0 = *reinterpret_cast<const bf16x8*>(Ks + kswz<64>(r32, cb));
;         const bf16x8 b1 = *reinterpret_cast<const bf16x8*>(Ks + kswz<64>(32 + r32, cb));
;         if (d0 == 0) { p0 = __builtin_amdgcn_mfma_f32_32x32x16_bf16(b0, qr[0], cinit, 0, 0, 0); p1 = __builtin_amdgcn_mfma_f32_32x32x16_bf16(b1, qr[0], cinit, 0, 0, 0); }
;         else { p0 = __builtin_amdgcn_mfma_f32_32x32x16_bf16(b0, qr[d0], p0, 0, 0, 0); p1 = __builtin_amdgcn_mfma_f32_32x32x16_bf16(b1, qr[d0], p1, 0, 0, 0); } }
; }
.LBB0_823:
	v_lshl_add_u64 v[202:203], v[200:201], 0, s[64:65]
	s_mov_b32 s2, 0x8a40000
	v_add_co_u32_e32 v64, vcc, s2, v202
	s_mov_b32 s2, 0x8a50000
	s_nop 0
	v_addc_co_u32_e32 v65, vcc, 0, v203, vcc
	v_add_co_u32_e32 v66, vcc, s2, v202
	v_lshl_add_u64 v[204:205], v[198:199], 0, s[64:65]
	s_nop 0
	v_addc_co_u32_e32 v67, vcc, 0, v203, vcc
	s_mov_b32 s2, 0x6a40000
	global_load_dwordx4 v[178:181], v[64:65], off
	global_load_dwordx4 v[182:185], v[66:67], off
	v_add_co_u32_e32 v64, vcc, s2, v204
	s_nop 1
	v_addc_co_u32_e32 v65, vcc, 0, v205, vcc
	global_load_dwordx4 v[186:189], v[64:65], off
	s_lshl_b32 s2, s42, 13
	s_add_i32 s2, s2, 0
	v_add_u32_e32 v128, s2, v223
	ds_read_b128 v[144:147], v128 offset:49152
	v_add_u32_e32 v129, s2, v226
	ds_read_b128 v[148:151], v129 offset:49152
	v_add_u32_e32 v130, s2, v228
	ds_read_b128 v[152:155], v130 offset:49152
	v_add_u32_e32 v131, s2, v229
	ds_read_b128 v[156:159], v131 offset:49152
	ds_read_b128 v[232:235], v128 offset:53248
	ds_read_b128 v[236:239], v129 offset:53248
	ds_read_b128 v[240:243], v130 offset:53248
	ds_read_b128 v[244:247], v131 offset:53248
	v_exp_f32_e32 v190, v120
	v_exp_f32_e32 v191, v121
	v_add_f32_e32 v120, v96, v97
	v_add_f32_e32 v121, v98, v99
	s_waitcnt lgkmcnt(7)
	v_mfma_f32_32x32x16_bf16 v[128:143], v[144:147], v[162:165], v[80:95]
	v_exp_f32_e32 v192, v122
	v_add_f32_e32 v120, v120, v121
	v_add_f32_e32 v121, v100, v101
	v_add_f32_e32 v122, v102, v103
	v_exp_f32_e32 v193, v123
	s_waitcnt lgkmcnt(6)
	v_mfma_f32_32x32x16_bf16 v[128:143], v[148:151], v[166:169], v[128:143]
	v_add_f32_e32 v121, v121, v122
	v_add_f32_e32 v122, v104, v105
	v_add_f32_e32 v123, v106, v107
	v_add_f32_e32 v122, v122, v123
	v_add_f32_e32 v123, v108, v109
	s_waitcnt lgkmcnt(5)
	v_mfma_f32_32x32x16_bf16 v[128:143], v[152:155], v[170:173], v[128:143]
	v_add_f32_e32 v208, v110, v111
	v_add_f32_e32 v123, v123, v208
	v_add_f32_e32 v208, v112, v113
	v_add_f32_e32 v209, v114, v115
	v_add_f32_e32 v208, v208, v209
	s_waitcnt lgkmcnt(4)
	v_mfma_f32_32x32x16_bf16 v[128:143], v[156:159], v[174:177], v[128:143]
	v_exp_f32_e32 v124, v124
	v_exp_f32_e32 v125, v125
	s_waitcnt lgkmcnt(3)
	v_mfma_f32_32x32x16_bf16 v[144:159], v[232:235], v[162:165], v[80:95]
	v_exp_f32_e32 v126, v126
	v_exp_f32_e32 v127, v127
	v_add_f32_e32 v120, v208, v120
	v_add_f32_e32 v208, v116, v117
	v_add_f32_e32 v209, v118, v119
	v_add_f32_e32 v208, v208, v209
	v_add_f32_e32 v121, v208, v121
	s_waitcnt lgkmcnt(2)
	v_mfma_f32_32x32x16_bf16 v[144:159], v[236:239], v[166:169], v[144:159]
	v_add_f32_e32 v208, v190, v191
	v_add_f32_e32 v209, v192, v193
	v_add_f32_e32 v208, v208, v209
	v_add_f32_e32 v122, v122, v208
	v_add_f32_e32 v208, v124, v125
	v_add_f32_e32 v209, v126, v127
	v_add_f32_e32 v208, v208, v209
	s_waitcnt lgkmcnt(1)
	v_mfma_f32_32x32x16_bf16 v[144:159], v[240:243], v[170:173], v[144:159]
	v_add_f32_e32 v123, v123, v208
	v_add_f32_e32 v120, v120, v121
	v_add_f32_e32 v121, v122, v123
	v_add_f32_e32 v231, v120, v121
	v_mov_b32_e32 v232, v231
	v_cvt_pk_bf16_f32 v96, v96, v97
	v_cvt_pk_bf16_f32 v97, v98, v99
	s_waitcnt lgkmcnt(0)
	v_mfma_f32_32x32x16_bf16 v[144:159], v[244:247], v[174:177], v[144:159]
	v_cvt_pk_bf16_f32 v98, v100, v101
	v_cvt_pk_bf16_f32 v99, v102, v103
	v_cvt_pk_bf16_f32 v120, v104, v105
	v_cvt_pk_bf16_f32 v121, v106, v107
	v_cvt_pk_bf16_f32 v122, v108, v109
	v_cvt_pk_bf16_f32 v123, v110, v111
	v_cvt_pk_bf16_f32 v104, v112, v113
	v_cvt_pk_bf16_f32 v105, v114, v115
	v_cvt_pk_bf16_f32 v106, v116, v117
	v_cvt_pk_bf16_f32 v107, v118, v119
	v_cvt_pk_bf16_f32 v100, v190, v191
	v_cvt_pk_bf16_f32 v101, v192, v193
	v_cvt_pk_bf16_f32 v102, v124, v125
	v_cvt_pk_bf16_f32 v103, v126, v127
	s_nop 0
	v_permlane32_swap_b32_e32 v231, v232
	v_permlane32_swap_b32_e32 v96, v98
	v_permlane32_swap_b32_e32 v97, v99
	v_permlane32_swap_b32_e32 v120, v122
	v_permlane32_swap_b32_e32 v121, v123
	v_permlane32_swap_b32_e32 v104, v106
	v_permlane32_swap_b32_e32 v105, v107
	v_permlane32_swap_b32_e32 v100, v102
	v_permlane32_swap_b32_e32 v101, v103
	v_lshl_add_u32 v234, s12, 14, v217
	ds_read_b64_tr_b16 v[108:109], v234 offset:0
	ds_read_b64_tr_b16 v[110:111], v234 offset:0x800
	ds_read_b64_tr_b16 v[112:113], v234 offset:0x1000
	ds_read_b64_tr_b16 v[114:115], v234 offset:0x1800
	ds_read_b64_tr_b16 v[116:117], v234 offset:0x2000
	ds_read_b64_tr_b16 v[118:119], v234 offset:0x2800
	ds_read_b64_tr_b16 v[124:125], v234 offset:0x3000
	ds_read_b64_tr_b16 v[126:127], v234 offset:0x3800
	ds_read_b64_tr_b16 v[236:237], v234 offset:0x200
	ds_read_b64_tr_b16 v[238:239], v234 offset:0xa00
	ds_read_b64_tr_b16 v[240:241], v234 offset:0x1200
	ds_read_b64_tr_b16 v[242:243], v234 offset:0x1a00
	ds_read_b64_tr_b16 v[244:245], v234 offset:0x2200
	ds_read_b64_tr_b16 v[246:247], v234 offset:0x2a00
	ds_read_b64_tr_b16 v[190:191], v234 offset:0x3200
	ds_read_b64_tr_b16 v[192:193], v234 offset:0x3a00
	s_waitcnt lgkmcnt(8)
	s_nop 0
	v_mfma_f32_32x32x16_bf16 v[0:15], v[96:99], v[108:111], v[0:15]
	v_max_f32_e32 v108, v128, v129
	v_max3_f32 v109, v130, v131, v145
	v_max3_f32 v108, v108, v144, v146
	v_max3_f32 v108, v108, v147, v132
	v_max3_f32 v109, v109, v134, v135
	v_mfma_f32_32x32x16_bf16 v[0:15], v[120:123], v[112:115], v[0:15]
	v_max3_f32 v208, v108, v133, v148
	v_max3_f32 v209, v109, v150, v151
	v_mfma_f32_32x32x16_bf16 v[0:15], v[104:107], v[116:119], v[0:15]
	v_mfma_f32_32x32x16_bf16 v[0:15], v[100:103], v[124:127], v[0:15]
	ds_read_b64_tr_b16 v[124:125], v234 offset:0x400
	ds_read_b64_tr_b16 v[126:127], v234 offset:0xc00
	ds_read_b64_tr_b16 v[116:117], v234 offset:0x1400
	ds_read_b64_tr_b16 v[118:119], v234 offset:0x1c00
	ds_read_b64_tr_b16 v[112:113], v234 offset:0x2400
	ds_read_b64_tr_b16 v[114:115], v234 offset:0x2c00
	ds_read_b64_tr_b16 v[108:109], v234 offset:0x3400
	ds_read_b64_tr_b16 v[110:111], v234 offset:0x3c00
	s_waitcnt lgkmcnt(8)
	v_mfma_f32_32x32x16_bf16 v[48:63], v[96:99], v[236:239], v[48:63]
	v_max3_f32 v208, v208, v149, v136
	v_max3_f32 v209, v209, v138, v139
	v_max3_f32 v208, v208, v137, v152
	v_max3_f32 v209, v209, v154, v155
	v_max3_f32 v208, v208, v153, v140
	v_max3_f32 v209, v209, v142, v143
	v_max3_f32 v208, v208, v141, v156
	v_mfma_f32_32x32x16_bf16 v[48:63], v[120:123], v[240:243], v[48:63]
	v_max3_f32 v209, v209, v158, v159
	v_max3_f32 v208, v208, v157, v209
	v_mov_b32_e32 v209, v208
	s_nop 1
	v_permlane32_swap_b32_e32 v208, v209
	v_mfma_f32_32x32x16_bf16 v[48:63], v[104:107], v[244:247], v[48:63]
	v_max_f32_e32 v233, v208, v209
	v_mfma_f32_32x32x16_bf16 v[48:63], v[100:103], v[190:193], v[48:63]
	s_mov_b32 s2, 0x4138aa3b
	v_cmp_ge_f32_e32 vcc, s2, v233
	s_cmp_eq_u64 vcc, exec
	s_cbranch_scc0 .LBB0_836
	v_mov_b32_e32 v233, 1.0

; __device__ __forceinline__ void qkt64c(f32x16& p0, f32x16& p1, const char* Ks, const bf16x8* qr, const f32x16& cinit, int r32, int hi) {
; #pragma unroll
;     for (int d0 = 0; d0 < 4; ++d0) { const int cb = (d0 * 16 + hi * 8) * 2;
;         const bf16x8 b0 = *reinterpret_cast<const bf16x8*>(Ks + kswz<64>(r32, cb));
;         const bf16x8 b1 = *reinterpret_cast<const bf16x8*>(Ks + kswz<64>(32 + r32, cb));
;         if (d0 == 0) { p0 = __builtin_amdgcn_mfma_f32_32x32x16_bf16(b0, qr[0], cinit, 0, 0, 0); p1 = __builtin_amdgcn_mfma_f32_32x32x16_bf16(b1, qr[0], cinit, 0, 0, 0); }
;         else { p0 = __builtin_amdgcn_mfma_f32_32x32x16_bf16(b0, qr[d0], p0, 0, 0, 0); p1 = __builtin_amdgcn_mfma_f32_32x32x16_bf16(b1, qr[d0], p1, 0, 0, 0); } }
; }
.LBB0_829:
	v_add_co_u32_e32 v96, vcc, 0x8a60000, v202
	s_waitcnt lgkmcnt(0)
	s_nop 0
	v_addc_co_u32_e32 v97, vcc, 0, v203, vcc
	v_add_co_u32_e32 v98, vcc, 0x8a70000, v202
	s_barrier
	s_nop 0
	v_addc_co_u32_e32 v99, vcc, 0, v203, vcc
	global_load_dwordx4 v[178:181], v[96:97], off
	global_load_dwordx4 v[182:185], v[98:99], off
	v_add_co_u32_e32 v96, vcc, 0x6a60000, v204
	s_nop 1
	v_addc_co_u32_e32 v97, vcc, 0, v205, vcc
	global_load_dwordx4 v[186:189], v[96:97], off
	v_add_u32_e32 v96, s2, v223
	ds_read_b128 v[112:115], v96 offset:49152
	v_add_u32_e32 v97, s2, v226
	ds_read_b128 v[116:119], v97 offset:49152
	v_add_u32_e32 v98, s2, v228
	ds_read_b128 v[120:123], v98 offset:49152
	v_add_u32_e32 v99, s2, v229
	ds_read_b128 v[124:127], v99 offset:49152
	ds_read_b128 v[190:193], v96 offset:53248
	ds_read_b128 v[202:205], v97 offset:53248
	ds_read_b128 v[234:237], v98 offset:53248
	ds_read_b128 v[238:241], v99 offset:53248
	v_exp_f32_e32 v208, v152
	v_exp_f32_e32 v209, v153
	v_add_f32_e32 v152, v128, v129
	v_add_f32_e32 v153, v130, v131
	s_waitcnt lgkmcnt(7)
	v_mfma_f32_32x32x16_bf16 v[96:111], v[112:115], v[162:165], v[80:95]
	v_exp_f32_e32 v210, v154
	v_add_f32_e32 v152, v152, v153
	v_add_f32_e32 v153, v132, v133
	v_add_f32_e32 v154, v134, v135
	v_exp_f32_e32 v211, v155
	s_waitcnt lgkmcnt(6)
	v_mfma_f32_32x32x16_bf16 v[96:111], v[116:119], v[166:169], v[96:111]
	v_add_f32_e32 v153, v153, v154
	v_add_f32_e32 v154, v136, v137
	v_add_f32_e32 v155, v138, v139
	v_add_f32_e32 v154, v154, v155
	v_add_f32_e32 v155, v140, v141
	s_waitcnt lgkmcnt(5)
	v_mfma_f32_32x32x16_bf16 v[96:111], v[120:123], v[170:173], v[96:111]
	v_exp_f32_e32 v156, v156
	v_exp_f32_e32 v157, v157
	v_exp_f32_e32 v158, v158
	v_exp_f32_e32 v159, v159
	s_waitcnt lgkmcnt(4)
	v_mfma_f32_32x32x16_bf16 v[96:111], v[124:127], v[174:177], v[96:111]
	s_waitcnt lgkmcnt(3)
	v_mfma_f32_32x32x16_bf16 v[112:127], v[190:193], v[162:165], v[80:95]
	v_add_f32_e32 v190, v142, v143
	v_add_f32_e32 v155, v155, v190
	v_add_f32_e32 v190, v144, v145
	v_add_f32_e32 v191, v146, v147
	v_add_f32_e32 v190, v190, v191
	v_add_f32_e32 v152, v152, v190
	v_add_f32_e32 v190, v148, v149
	s_waitcnt lgkmcnt(2)
	v_mfma_f32_32x32x16_bf16 v[112:127], v[202:205], v[166:169], v[112:127]
	v_add_f32_e32 v191, v150, v151
	v_add_f32_e32 v190, v190, v191
	v_add_f32_e32 v153, v153, v190
	v_add_f32_e32 v190, v208, v209
	v_add_f32_e32 v191, v210, v211
	v_add_f32_e32 v190, v190, v191
	v_add_f32_e32 v154, v154, v190
	s_waitcnt lgkmcnt(1)
	v_mfma_f32_32x32x16_bf16 v[112:127], v[234:237], v[170:173], v[112:127]
	v_add_f32_e32 v190, v156, v157
	v_add_f32_e32 v191, v158, v159
	v_add_f32_e32 v190, v190, v191
	v_add_f32_e32 v155, v155, v190
	v_add_f32_e32 v152, v152, v153
	v_add_f32_e32 v153, v154, v155
	v_add_f32_e32 v203, v152, v153
	s_waitcnt lgkmcnt(0)
	v_mfma_f32_32x32x16_bf16 v[112:127], v[238:241], v[174:177], v[112:127]
	v_mov_b32_e32 v204, v203
	v_cvt_pk_bf16_f32 v152, v128, v129
	v_cvt_pk_bf16_f32 v153, v130, v131
	v_cvt_pk_bf16_f32 v154, v132, v133
	v_cvt_pk_bf16_f32 v155, v134, v135
	v_cvt_pk_bf16_f32 v136, v136, v137
	v_cvt_pk_bf16_f32 v137, v138, v139
	v_cvt_pk_bf16_f32 v138, v140, v141
	v_cvt_pk_bf16_f32 v139, v142, v143
	v_cvt_pk_bf16_f32 v132, v144, v145
	v_cvt_pk_bf16_f32 v133, v146, v147
	v_cvt_pk_bf16_f32 v134, v148, v149
	v_cvt_pk_bf16_f32 v135, v150, v151
	v_cvt_pk_bf16_f32 v128, v208, v209
	v_cvt_pk_bf16_f32 v129, v210, v211
	v_cvt_pk_bf16_f32 v130, v156, v157
	v_cvt_pk_bf16_f32 v131, v158, v159
	s_nop 1
	v_permlane32_swap_b32_e32 v203, v204
	v_permlane32_swap_b32_e32 v152, v154
	v_permlane32_swap_b32_e32 v153, v155
	v_permlane32_swap_b32_e32 v136, v138
	v_permlane32_swap_b32_e32 v137, v139
	v_permlane32_swap_b32_e32 v132, v134
	v_permlane32_swap_b32_e32 v133, v135
	v_permlane32_swap_b32_e32 v128, v130
	v_permlane32_swap_b32_e32 v129, v131
	v_lshl_add_u32 v205, s42, 14, v217
	ds_read_b64_tr_b16 v[140:141], v205 offset:0
	ds_read_b64_tr_b16 v[142:143], v205 offset:0x800
	ds_read_b64_tr_b16 v[144:145], v205 offset:0x1000
	ds_read_b64_tr_b16 v[146:147], v205 offset:0x1800
	ds_read_b64_tr_b16 v[148:149], v205 offset:0x2000
	ds_read_b64_tr_b16 v[150:151], v205 offset:0x2800
	ds_read_b64_tr_b16 v[156:157], v205 offset:0x3000
	ds_read_b64_tr_b16 v[158:159], v205 offset:0x3800
	ds_read_b64_tr_b16 v[190:191], v205 offset:0x200
	ds_read_b64_tr_b16 v[192:193], v205 offset:0xa00
	ds_read_b64_tr_b16 v[234:235], v205 offset:0x1200
	ds_read_b64_tr_b16 v[236:237], v205 offset:0x1a00
	ds_read_b64_tr_b16 v[238:239], v205 offset:0x2200
	ds_read_b64_tr_b16 v[240:241], v205 offset:0x2a00
	ds_read_b64_tr_b16 v[242:243], v205 offset:0x3200
	ds_read_b64_tr_b16 v[244:245], v205 offset:0x3a00
	s_waitcnt lgkmcnt(8)
	s_nop 0
	v_mfma_f32_32x32x16_bf16 v[0:15], v[152:155], v[140:143], v[0:15]
	v_max_f32_e32 v140, v96, v97
	v_max3_f32 v140, v140, v112, v114
	v_max3_f32 v141, v98, v99, v113
	v_max3_f32 v140, v140, v115, v100
	v_max3_f32 v141, v141, v102, v103
	v_mfma_f32_32x32x16_bf16 v[0:15], v[136:139], v[144:147], v[0:15]
	v_max3_f32 v202, v140, v101, v116
	v_max3_f32 v208, v141, v118, v119
	v_mfma_f32_32x32x16_bf16 v[0:15], v[132:135], v[148:151], v[0:15]
	v_mfma_f32_32x32x16_bf16 v[0:15], v[128:131], v[156:159], v[0:15]
	ds_read_b64_tr_b16 v[156:157], v205 offset:0x400
	ds_read_b64_tr_b16 v[158:159], v205 offset:0xc00
	ds_read_b64_tr_b16 v[148:149], v205 offset:0x1400
	ds_read_b64_tr_b16 v[150:151], v205 offset:0x1c00
	ds_read_b64_tr_b16 v[144:145], v205 offset:0x2400
	ds_read_b64_tr_b16 v[146:147], v205 offset:0x2c00
	ds_read_b64_tr_b16 v[140:141], v205 offset:0x3400
	ds_read_b64_tr_b16 v[142:143], v205 offset:0x3c00
	s_waitcnt lgkmcnt(8)
	v_mfma_f32_32x32x16_bf16 v[48:63], v[152:155], v[190:193], v[48:63]
	v_max3_f32 v190, v202, v117, v104
	v_max3_f32 v191, v208, v106, v107
	v_max3_f32 v190, v190, v105, v120
	v_max3_f32 v191, v191, v122, v123
	v_max3_f32 v190, v190, v121, v108
	v_max3_f32 v191, v191, v110, v111
	v_max3_f32 v190, v190, v109, v124
	v_mfma_f32_32x32x16_bf16 v[48:63], v[136:139], v[234:237], v[48:63]
	v_max3_f32 v191, v191, v126, v127
	v_max3_f32 v190, v190, v125, v191
	v_mov_b32_e32 v191, v190
	s_nop 1
	v_permlane32_swap_b32_e32 v190, v191
	v_mfma_f32_32x32x16_bf16 v[48:63], v[132:135], v[238:241], v[48:63]
	v_max_f32_e32 v234, v190, v191
	v_mfma_f32_32x32x16_bf16 v[48:63], v[128:131], v[242:245], v[48:63]
	s_mov_b32 s2, 0x4138aa3b
	v_cmp_ge_f32_e32 vcc, s2, v234
	s_cmp_eq_u64 vcc, exec
	v_mov_b32_e32 v202, 1.0
	s_cbranch_scc0 .LBB0_837

; __device__ __forceinline__ void qkt64c(f32x16& p0, f32x16& p1, const char* Ks, const bf16x8* qr, const f32x16& cinit, int r32, int hi) {
; #pragma unroll
;     for (int d0 = 0; d0 < 4; ++d0) { const int cb = (d0 * 16 + hi * 8) * 2;
;         const bf16x8 b0 = *reinterpret_cast<const bf16x8*>(Ks + kswz<64>(r32, cb));
;         const bf16x8 b1 = *reinterpret_cast<const bf16x8*>(Ks + kswz<64>(32 + r32, cb));
;         if (d0 == 0) { p0 = __builtin_amdgcn_mfma_f32_32x32x16_bf16(b0, qr[0], cinit, 0, 0, 0); p1 = __builtin_amdgcn_mfma_f32_32x32x16_bf16(b1, qr[0], cinit, 0, 0, 0); }
;         else { p0 = __builtin_amdgcn_mfma_f32_32x32x16_bf16(b0, qr[d0], p0, 0, 0, 0); p1 = __builtin_amdgcn_mfma_f32_32x32x16_bf16(b1, qr[d0], p1, 0, 0, 0); } }
; }
.LBB0_846:
	v_lshl_add_u64 v[202:203], v[200:201], 0, s[64:65]
	s_mov_b32 s2, 0x8a40000
	v_add_co_u32_e32 v64, vcc, s2, v202
	s_mov_b32 s2, 0x8a50000
	s_nop 0
	v_addc_co_u32_e32 v65, vcc, 0, v203, vcc
	v_add_co_u32_e32 v66, vcc, s2, v202
	v_lshl_add_u64 v[204:205], v[198:199], 0, s[64:65]
	s_nop 0
	v_addc_co_u32_e32 v67, vcc, 0, v203, vcc
	s_mov_b32 s2, 0x6a40000
	global_load_dwordx4 v[178:181], v[64:65], off
	global_load_dwordx4 v[182:185], v[66:67], off
	v_add_co_u32_e32 v64, vcc, s2, v204
	s_nop 1
	v_addc_co_u32_e32 v65, vcc, 0, v205, vcc
	global_load_dwordx4 v[186:189], v[64:65], off offset:128
	s_lshl_b32 s2, s30, 13
	s_add_i32 s2, s2, 0
	v_add_u32_e32 v128, s2, v227
	ds_read_b128 v[144:147], v128 offset:49152
	v_add_u32_e32 v129, s2, v231
	ds_read_b128 v[148:151], v129 offset:49152
	v_add_u32_e32 v130, s2, v232
	ds_read_b128 v[152:155], v130 offset:49152
	v_add_u32_e32 v131, s2, v233
	ds_read_b128 v[156:159], v131 offset:49152
	ds_read_b128 v[190:193], v128 offset:53248
	ds_read_b128 v[236:239], v129 offset:53248
	ds_read_b128 v[240:243], v130 offset:53248
	ds_read_b128 v[244:247], v131 offset:53248
	v_exp_f32_e32 v208, v120
	v_exp_f32_e32 v209, v121
	v_add_f32_e32 v120, v96, v97
	v_add_f32_e32 v121, v98, v99
	s_waitcnt lgkmcnt(7)
	v_mfma_f32_32x32x16_bf16 v[128:143], v[144:147], v[162:165], v[80:95]
	v_exp_f32_e32 v210, v122
	v_add_f32_e32 v120, v120, v121
	v_add_f32_e32 v121, v100, v101
	v_add_f32_e32 v122, v102, v103
	v_exp_f32_e32 v211, v123
	s_waitcnt lgkmcnt(6)
	v_mfma_f32_32x32x16_bf16 v[128:143], v[148:151], v[166:169], v[128:143]
	v_add_f32_e32 v121, v121, v122
	v_add_f32_e32 v122, v104, v105
	v_add_f32_e32 v123, v106, v107
	v_add_f32_e32 v122, v122, v123
	v_add_f32_e32 v123, v108, v109
	s_waitcnt lgkmcnt(5)
	v_mfma_f32_32x32x16_bf16 v[128:143], v[152:155], v[170:173], v[128:143]
	v_exp_f32_e32 v124, v124
	v_exp_f32_e32 v125, v125
	v_exp_f32_e32 v126, v126
	v_exp_f32_e32 v127, v127
	v_cvt_pk_bf16_f32 v96, v96, v97
	s_waitcnt lgkmcnt(4)
	v_mfma_f32_32x32x16_bf16 v[128:143], v[156:159], v[174:177], v[128:143]
	v_cvt_pk_bf16_f32 v97, v98, v99
	v_cvt_pk_bf16_f32 v98, v100, v101
	v_cvt_pk_bf16_f32 v99, v102, v103
	s_nop 0
	v_permlane32_swap_b32_e32 v96, v98
	s_waitcnt lgkmcnt(3)
	v_mfma_f32_32x32x16_bf16 v[144:159], v[190:193], v[162:165], v[80:95]
	v_add_f32_e32 v190, v110, v111
	v_add_f32_e32 v123, v123, v190
	v_add_f32_e32 v190, v112, v113
	v_add_f32_e32 v191, v114, v115
	v_add_f32_e32 v190, v190, v191
	v_add_f32_e32 v120, v190, v120
	v_add_f32_e32 v190, v116, v117
	s_waitcnt lgkmcnt(2)
	v_mfma_f32_32x32x16_bf16 v[144:159], v[236:239], v[166:169], v[144:159]
	v_add_f32_e32 v191, v118, v119
	v_add_f32_e32 v190, v190, v191
	v_add_f32_e32 v121, v190, v121
	v_add_f32_e32 v190, v208, v209
	v_add_f32_e32 v191, v210, v211
	v_add_f32_e32 v190, v190, v191
	v_add_f32_e32 v122, v122, v190
	s_waitcnt lgkmcnt(1)
	v_mfma_f32_32x32x16_bf16 v[144:159], v[240:243], v[170:173], v[144:159]
	v_add_f32_e32 v190, v124, v125
	v_add_f32_e32 v191, v126, v127
	v_add_f32_e32 v190, v190, v191
	v_add_f32_e32 v123, v123, v190
	v_add_f32_e32 v120, v120, v121
	v_add_f32_e32 v121, v122, v123
	v_add_f32_e32 v235, v120, v121
	s_waitcnt lgkmcnt(0)
	v_mfma_f32_32x32x16_bf16 v[144:159], v[244:247], v[174:177], v[144:159]
	v_mov_b32_e32 v236, v235
	v_cvt_pk_bf16_f32 v120, v104, v105
	v_cvt_pk_bf16_f32 v121, v106, v107
	v_cvt_pk_bf16_f32 v122, v108, v109
	v_cvt_pk_bf16_f32 v123, v110, v111
	v_cvt_pk_bf16_f32 v104, v112, v113
	v_cvt_pk_bf16_f32 v105, v114, v115
	v_cvt_pk_bf16_f32 v106, v116, v117
	v_cvt_pk_bf16_f32 v107, v118, v119
	v_cvt_pk_bf16_f32 v100, v208, v209
	v_cvt_pk_bf16_f32 v101, v210, v211
	v_cvt_pk_bf16_f32 v102, v124, v125
	v_cvt_pk_bf16_f32 v103, v126, v127
	s_nop 1
	v_permlane32_swap_b32_e32 v235, v236
	v_permlane32_swap_b32_e32 v97, v99
	v_permlane32_swap_b32_e32 v120, v122
	v_permlane32_swap_b32_e32 v121, v123
	v_permlane32_swap_b32_e32 v104, v106
	v_permlane32_swap_b32_e32 v105, v107
	v_permlane32_swap_b32_e32 v100, v102
	v_permlane32_swap_b32_e32 v101, v103
	v_lshl_add_u32 v238, s12, 14, v221
	ds_read_b64_tr_b16 v[108:109], v238 offset:0
	ds_read_b64_tr_b16 v[110:111], v238 offset:0x800
	ds_read_b64_tr_b16 v[112:113], v238 offset:0x1000
	ds_read_b64_tr_b16 v[114:115], v238 offset:0x1800
	ds_read_b64_tr_b16 v[116:117], v238 offset:0x2000
	ds_read_b64_tr_b16 v[118:119], v238 offset:0x2800
	ds_read_b64_tr_b16 v[124:125], v238 offset:0x3000
	ds_read_b64_tr_b16 v[126:127], v238 offset:0x3800
	ds_read_b64_tr_b16 v[190:191], v238 offset:0x200
	ds_read_b64_tr_b16 v[192:193], v238 offset:0xa00
	ds_read_b64_tr_b16 v[240:241], v238 offset:0x1200
	ds_read_b64_tr_b16 v[242:243], v238 offset:0x1a00
	ds_read_b64_tr_b16 v[244:245], v238 offset:0x2200
	ds_read_b64_tr_b16 v[246:247], v238 offset:0x2a00
	ds_read_b64_tr_b16 v[208:209], v238 offset:0x3200
	ds_read_b64_tr_b16 v[210:211], v238 offset:0x3a00
	s_waitcnt lgkmcnt(8)
	s_nop 0
	v_mfma_f32_32x32x16_bf16 v[0:15], v[96:99], v[108:111], v[0:15]
	v_max_f32_e32 v108, v128, v129
	v_max3_f32 v108, v108, v144, v146
	v_max3_f32 v109, v130, v131, v145
	v_max3_f32 v108, v108, v147, v132
	v_max3_f32 v109, v109, v134, v135
	v_mfma_f32_32x32x16_bf16 v[0:15], v[120:123], v[112:115], v[0:15]
	v_max3_f32 v237, v108, v133, v148
	v_max3_f32 v239, v109, v150, v151
	v_mfma_f32_32x32x16_bf16 v[0:15], v[104:107], v[116:119], v[0:15]
	v_mfma_f32_32x32x16_bf16 v[0:15], v[100:103], v[124:127], v[0:15]
	ds_read_b64_tr_b16 v[124:125], v238 offset:0x400
	ds_read_b64_tr_b16 v[126:127], v238 offset:0xc00
	ds_read_b64_tr_b16 v[116:117], v238 offset:0x1400
	ds_read_b64_tr_b16 v[118:119], v238 offset:0x1c00
	ds_read_b64_tr_b16 v[112:113], v238 offset:0x2400
	ds_read_b64_tr_b16 v[114:115], v238 offset:0x2c00
	ds_read_b64_tr_b16 v[108:109], v238 offset:0x3400
	ds_read_b64_tr_b16 v[110:111], v238 offset:0x3c00
	s_waitcnt lgkmcnt(8)
	v_mfma_f32_32x32x16_bf16 v[48:63], v[96:99], v[190:193], v[48:63]
	v_max3_f32 v190, v237, v149, v136
	v_max3_f32 v191, v239, v138, v139
	v_max3_f32 v190, v190, v137, v152
	v_max3_f32 v191, v191, v154, v155
	v_max3_f32 v190, v190, v153, v140
	v_max3_f32 v191, v191, v142, v143
	v_max3_f32 v190, v190, v141, v156
	v_mfma_f32_32x32x16_bf16 v[48:63], v[120:123], v[240:243], v[48:63]
	v_max3_f32 v191, v191, v158, v159
	v_max3_f32 v190, v190, v157, v191
	v_mov_b32_e32 v191, v190
	s_nop 1
	v_permlane32_swap_b32_e32 v190, v191
	v_mfma_f32_32x32x16_bf16 v[48:63], v[104:107], v[244:247], v[48:63]
	v_max_f32_e32 v237, v190, v191
	v_mfma_f32_32x32x16_bf16 v[48:63], v[100:103], v[208:211], v[48:63]
	s_mov_b32 s2, 0x4138aa3b
	v_cmp_ge_f32_e32 vcc, s2, v237
	s_cmp_eq_u64 vcc, exec
	s_cbranch_scc0 .LBB0_859
	v_mov_b32_e32 v237, 1.0

; __device__ __forceinline__ void qkt64c(f32x16& p0, f32x16& p1, const char* Ks, const bf16x8* qr, const f32x16& cinit, int r32, int hi) {
; #pragma unroll
;     for (int d0 = 0; d0 < 4; ++d0) { const int cb = (d0 * 16 + hi * 8) * 2;
;         const bf16x8 b0 = *reinterpret_cast<const bf16x8*>(Ks + kswz<64>(r32, cb));
;         const bf16x8 b1 = *reinterpret_cast<const bf16x8*>(Ks + kswz<64>(32 + r32, cb));
;         if (d0 == 0) { p0 = __builtin_amdgcn_mfma_f32_32x32x16_bf16(b0, qr[0], cinit, 0, 0, 0); p1 = __builtin_amdgcn_mfma_f32_32x32x16_bf16(b1, qr[0], cinit, 0, 0, 0); }
;         else { p0 = __builtin_amdgcn_mfma_f32_32x32x16_bf16(b0, qr[d0], p0, 0, 0, 0); p1 = __builtin_amdgcn_mfma_f32_32x32x16_bf16(b1, qr[d0], p1, 0, 0, 0); } }
; }
.LBB0_852:
	v_add_co_u32_e32 v96, vcc, 0x8a60000, v202
	s_waitcnt lgkmcnt(0)
	s_nop 0
	v_addc_co_u32_e32 v97, vcc, 0, v203, vcc
	v_add_co_u32_e32 v98, vcc, 0x8a70000, v202
	s_barrier
	s_nop 0
	v_addc_co_u32_e32 v99, vcc, 0, v203, vcc
	global_load_dwordx4 v[178:181], v[96:97], off
	global_load_dwordx4 v[182:185], v[98:99], off
	v_add_co_u32_e32 v96, vcc, 0x6a60000, v204
	s_nop 1
	v_addc_co_u32_e32 v97, vcc, 0, v205, vcc
	global_load_dwordx4 v[186:189], v[96:97], off offset:128
	v_add_u32_e32 v96, s2, v227
	ds_read_b128 v[112:115], v96 offset:49152
	v_add_u32_e32 v97, s2, v231
	ds_read_b128 v[116:119], v97 offset:49152
	v_add_u32_e32 v98, s2, v232
	ds_read_b128 v[120:123], v98 offset:49152
	v_add_u32_e32 v99, s2, v233
	ds_read_b128 v[124:127], v99 offset:49152
	ds_read_b128 v[190:193], v96 offset:53248
	ds_read_b128 v[202:205], v97 offset:53248
	ds_read_b128 v[208:211], v98 offset:53248
	ds_read_b128 v[238:241], v99 offset:53248
	v_exp_f32_e32 v242, v152
	v_exp_f32_e32 v243, v153
	v_add_f32_e32 v152, v128, v129
	v_add_f32_e32 v153, v130, v131
	s_waitcnt lgkmcnt(7)
	v_mfma_f32_32x32x16_bf16 v[96:111], v[112:115], v[162:165], v[80:95]
	v_exp_f32_e32 v244, v154
	v_add_f32_e32 v152, v152, v153
	v_add_f32_e32 v153, v132, v133
	v_add_f32_e32 v154, v134, v135
	v_exp_f32_e32 v245, v155
	s_waitcnt lgkmcnt(6)
	v_mfma_f32_32x32x16_bf16 v[96:111], v[116:119], v[166:169], v[96:111]
	v_add_f32_e32 v153, v153, v154
	v_add_f32_e32 v154, v136, v137
	v_add_f32_e32 v155, v138, v139
	v_add_f32_e32 v154, v154, v155
	v_add_f32_e32 v155, v140, v141
	s_waitcnt lgkmcnt(5)
	v_mfma_f32_32x32x16_bf16 v[96:111], v[120:123], v[170:173], v[96:111]
	v_exp_f32_e32 v156, v156
	v_exp_f32_e32 v157, v157
	v_exp_f32_e32 v158, v158
	v_exp_f32_e32 v159, v159
	s_waitcnt lgkmcnt(4)
	v_mfma_f32_32x32x16_bf16 v[96:111], v[124:127], v[174:177], v[96:111]
	s_waitcnt lgkmcnt(3)
	v_mfma_f32_32x32x16_bf16 v[112:127], v[190:193], v[162:165], v[80:95]
	v_add_f32_e32 v190, v142, v143
	v_add_f32_e32 v155, v155, v190
	v_add_f32_e32 v190, v144, v145
	v_add_f32_e32 v191, v146, v147
	v_add_f32_e32 v190, v190, v191
	v_add_f32_e32 v152, v152, v190
	v_add_f32_e32 v190, v148, v149
	s_waitcnt lgkmcnt(2)
	v_mfma_f32_32x32x16_bf16 v[112:127], v[202:205], v[166:169], v[112:127]
	v_add_f32_e32 v191, v150, v151
	v_add_f32_e32 v190, v190, v191
	v_add_f32_e32 v153, v153, v190
	v_add_f32_e32 v190, v242, v243
	v_add_f32_e32 v191, v244, v245
	v_add_f32_e32 v190, v190, v191
	v_add_f32_e32 v154, v154, v190
	s_waitcnt lgkmcnt(1)
	v_mfma_f32_32x32x16_bf16 v[112:127], v[208:211], v[170:173], v[112:127]
	v_add_f32_e32 v190, v156, v157
	v_add_f32_e32 v191, v158, v159
	v_add_f32_e32 v190, v190, v191
	v_add_f32_e32 v155, v155, v190
	v_add_f32_e32 v152, v152, v153
	v_add_f32_e32 v153, v154, v155
	v_add_f32_e32 v203, v152, v153
	s_waitcnt lgkmcnt(0)
	v_mfma_f32_32x32x16_bf16 v[112:127], v[238:241], v[174:177], v[112:127]
	v_mov_b32_e32 v204, v203
	v_cvt_pk_bf16_f32 v152, v128, v129
	v_cvt_pk_bf16_f32 v153, v130, v131
	v_cvt_pk_bf16_f32 v154, v132, v133
	v_cvt_pk_bf16_f32 v155, v134, v135
	v_cvt_pk_bf16_f32 v136, v136, v137
	v_cvt_pk_bf16_f32 v137, v138, v139
	v_cvt_pk_bf16_f32 v138, v140, v141
	v_cvt_pk_bf16_f32 v139, v142, v143
	v_cvt_pk_bf16_f32 v132, v144, v145
	v_cvt_pk_bf16_f32 v133, v146, v147
	v_cvt_pk_bf16_f32 v134, v148, v149
	v_cvt_pk_bf16_f32 v135, v150, v151
	v_cvt_pk_bf16_f32 v128, v242, v243
	v_cvt_pk_bf16_f32 v129, v244, v245
	v_cvt_pk_bf16_f32 v130, v156, v157
	v_cvt_pk_bf16_f32 v131, v158, v159
	s_nop 1
	v_permlane32_swap_b32_e32 v203, v204
	v_permlane32_swap_b32_e32 v152, v154
	v_permlane32_swap_b32_e32 v153, v155
	v_permlane32_swap_b32_e32 v136, v138
	v_permlane32_swap_b32_e32 v137, v139
	v_permlane32_swap_b32_e32 v132, v134
	v_permlane32_swap_b32_e32 v133, v135
	v_permlane32_swap_b32_e32 v128, v130
	v_permlane32_swap_b32_e32 v129, v131
	v_lshl_add_u32 v205, s30, 14, v221
	ds_read_b64_tr_b16 v[140:141], v205 offset:0
	ds_read_b64_tr_b16 v[142:143], v205 offset:0x800
	ds_read_b64_tr_b16 v[144:145], v205 offset:0x1000
	ds_read_b64_tr_b16 v[146:147], v205 offset:0x1800
	ds_read_b64_tr_b16 v[148:149], v205 offset:0x2000
	ds_read_b64_tr_b16 v[150:151], v205 offset:0x2800
	ds_read_b64_tr_b16 v[156:157], v205 offset:0x3000
	ds_read_b64_tr_b16 v[158:159], v205 offset:0x3800
	ds_read_b64_tr_b16 v[190:191], v205 offset:0x200
	ds_read_b64_tr_b16 v[192:193], v205 offset:0xa00
	ds_read_b64_tr_b16 v[208:209], v205 offset:0x1200
	ds_read_b64_tr_b16 v[210:211], v205 offset:0x1a00
	ds_read_b64_tr_b16 v[238:239], v205 offset:0x2200
	ds_read_b64_tr_b16 v[240:241], v205 offset:0x2a00
	ds_read_b64_tr_b16 v[242:243], v205 offset:0x3200
	ds_read_b64_tr_b16 v[244:245], v205 offset:0x3a00
	s_waitcnt lgkmcnt(8)
	s_nop 0
	v_mfma_f32_32x32x16_bf16 v[0:15], v[152:155], v[140:143], v[0:15]
	v_max_f32_e32 v140, v96, v97
	v_max3_f32 v140, v140, v112, v114
	v_max3_f32 v141, v98, v99, v113
	v_max3_f32 v140, v140, v115, v100
	v_max3_f32 v141, v141, v102, v103
	v_mfma_f32_32x32x16_bf16 v[0:15], v[136:139], v[144:147], v[0:15]
	v_max3_f32 v202, v140, v101, v116
	v_max3_f32 v246, v141, v118, v119
	v_mfma_f32_32x32x16_bf16 v[0:15], v[132:135], v[148:151], v[0:15]
	v_mfma_f32_32x32x16_bf16 v[0:15], v[128:131], v[156:159], v[0:15]
	ds_read_b64_tr_b16 v[156:157], v205 offset:0x400
	ds_read_b64_tr_b16 v[158:159], v205 offset:0xc00
	ds_read_b64_tr_b16 v[148:149], v205 offset:0x1400
	ds_read_b64_tr_b16 v[150:151], v205 offset:0x1c00
	ds_read_b64_tr_b16 v[144:145], v205 offset:0x2400
	ds_read_b64_tr_b16 v[146:147], v205 offset:0x2c00
	ds_read_b64_tr_b16 v[140:141], v205 offset:0x3400
	ds_read_b64_tr_b16 v[142:143], v205 offset:0x3c00
	s_waitcnt lgkmcnt(8)
	v_mfma_f32_32x32x16_bf16 v[48:63], v[152:155], v[190:193], v[48:63]
	v_max3_f32 v190, v202, v117, v104
	v_max3_f32 v191, v246, v106, v107
	v_max3_f32 v190, v190, v105, v120
	v_max3_f32 v191, v191, v122, v123
	v_max3_f32 v190, v190, v121, v108
	v_max3_f32 v191, v191, v110, v111
	v_max3_f32 v190, v190, v109, v124
	v_mfma_f32_32x32x16_bf16 v[48:63], v[136:139], v[208:211], v[48:63]
	v_max3_f32 v191, v191, v126, v127
	v_max3_f32 v190, v190, v125, v191
	v_mov_b32_e32 v191, v190
	s_nop 1
	v_permlane32_swap_b32_e32 v190, v191
	v_mfma_f32_32x32x16_bf16 v[48:63], v[132:135], v[238:241], v[48:63]
	v_max_f32_e32 v238, v190, v191
	v_mfma_f32_32x32x16_bf16 v[48:63], v[128:131], v[242:245], v[48:63]
	s_mov_b32 s2, 0x4138aa3b
	v_cmp_ge_f32_e32 vcc, s2, v238
	s_cmp_eq_u64 vcc, exec
	v_mov_b32_e32 v202, 1.0
	s_cbranch_scc0 .LBB0_860
